# baseline (speedup 1.0000x reference)
.Lit7b:
	global_load_dwordx4 v[112:115], v164, s[24:25]
	v_mfma_f32_16x16x32_f16 v[120:123], v[16:19], v[116:119], 0
	v_mfma_f32_16x16x32_f16 v[124:127], v[20:23], v[116:119], 0
	v_cndmask_b32_e32 v158, 4, v158, vcc
	v_mfma_f32_16x16x32_f16 v[128:131], v[24:27], v[116:119], 0
	v_mfma_f32_16x16x32_f16 v[132:135], v[28:31], v[116:119], 0
	v_min3_i32 v160, v136, v137, v157
	v_min3_i32 v160, v138, v139, v160
	v_min3_i32 v160, v140, v141, v160
	v_min3_i32 v160, v142, v143, v160
	v_min3_i32 v160, v144, v145, v160
	v_min3_i32 v160, v146, v147, v160
	v_min3_i32 v160, v148, v149, v160
	v_min3_i32 v156, v150, v151, v160
	v_cmp_ge_i32_e32 vcc, v156, v157
	v_mfma_f32_16x16x32_f16 v[136:139], v[32:35], v[116:119], 0
	v_mfma_f32_16x16x32_f16 v[140:143], v[36:39], v[116:119], 0
	v_cndmask_b32_e32 v158, 5, v158, vcc
	v_add_u32_e32 v162, s40, v158
	v_lshl_or_b32 v162, v162, 2, v166
	v_mov_b32_e32 v163, v156
	ds_min_u64 v167, v[162:163] offset:17152
	v_mfma_f32_16x16x32_f16 v[144:147], v[40:43], v[116:119], 0
	v_mfma_f32_16x16x32_f16 v[148:151], v[44:47], v[116:119], 0
	v_min3_i32 v160, v120, v121, s41
	v_min3_i32 v160, v122, v123, v160
	v_min3_i32 v160, v124, v125, v160
	v_min3_i32 v160, v126, v127, v160
	v_min3_i32 v160, v128, v129, v160
	v_min3_i32 v160, v130, v131, v160
	v_min3_i32 v160, v132, v133, v160
	v_min3_i32 v157, v134, v135, v160
	v_mfma_f32_16x16x32_f16 v[120:123], v[48:51], v[116:119], 0
	v_mfma_f32_16x16x32_f16 v[124:127], v[52:55], v[116:119], 0
	v_mov_b32_e32 v158, 0
	v_mfma_f32_16x16x32_f16 v[128:131], v[56:59], v[116:119], 0
	v_mfma_f32_16x16x32_f16 v[132:135], v[60:63], v[116:119], 0
	v_min3_i32 v160, v136, v137, v157
	v_min3_i32 v160, v138, v139, v160
	v_min3_i32 v160, v140, v141, v160
	v_min3_i32 v160, v142, v143, v160
	v_min3_i32 v160, v144, v145, v160
	v_min3_i32 v160, v146, v147, v160
	v_min3_i32 v160, v148, v149, v160
	v_min3_i32 v156, v150, v151, v160
	v_cmp_ge_i32_e32 vcc, v156, v157
	v_mfma_f32_16x16x32_f16 v[136:139], v[64:67], v[116:119], 0
	v_mfma_f32_16x16x32_f16 v[140:143], v[68:71], v[116:119], 0
	v_cndmask_b32_e32 v158, 1, v158, vcc
	v_mfma_f32_16x16x32_f16 v[144:147], v[72:75], v[116:119], 0
	v_mfma_f32_16x16x32_f16 v[148:151], v[76:79], v[116:119], 0
	v_min3_i32 v160, v120, v121, v156
	v_min3_i32 v160, v122, v123, v160
	v_min3_i32 v160, v124, v125, v160
	v_min3_i32 v160, v126, v127, v160
	v_min3_i32 v160, v128, v129, v160
	v_min3_i32 v160, v130, v131, v160
	v_min3_i32 v160, v132, v133, v160
	v_min3_i32 v157, v134, v135, v160
	v_cmp_ge_i32_e32 vcc, v157, v156
	v_mfma_f32_16x16x32_f16 v[120:123], v[80:83], v[116:119], 0
	v_mfma_f32_16x16x32_f16 v[124:127], v[84:87], v[116:119], 0
	v_cndmask_b32_e32 v158, 2, v158, vcc
	v_mfma_f32_16x16x32_f16 v[128:131], v[88:91], v[116:119], 0
	v_mfma_f32_16x16x32_f16 v[132:135], v[92:95], v[116:119], 0
	v_min3_i32 v160, v136, v137, v157
	v_min3_i32 v160, v138, v139, v160
	v_min3_i32 v160, v140, v141, v160
	v_min3_i32 v160, v142, v143, v160
	v_min3_i32 v160, v144, v145, v160
	v_min3_i32 v160, v146, v147, v160
	v_min3_i32 v160, v148, v149, v160
	v_min3_i32 v156, v150, v151, v160
	v_cmp_ge_i32_e32 vcc, v156, v157
	v_mfma_f32_16x16x32_f16 v[136:139], v[96:99], v[116:119], 0
	v_mfma_f32_16x16x32_f16 v[140:143], v[100:103], v[116:119], 0
	v_cndmask_b32_e32 v158, 3, v158, vcc
	v_mfma_f32_16x16x32_f16 v[144:147], v[104:107], v[116:119], 0
	v_mfma_f32_16x16x32_f16 v[148:151], v[108:111], v[116:119], 0
	v_min3_i32 v160, v120, v121, v156
	v_min3_i32 v160, v122, v123, v160
	v_min3_i32 v160, v124, v125, v160
	v_min3_i32 v160, v126, v127, v160
	v_min3_i32 v160, v128, v129, v160
	v_min3_i32 v160, v130, v131, v160
	v_min3_i32 v160, v132, v133, v160
	v_min3_i32 v157, v134, v135, v160
	v_cmp_ge_i32_e32 vcc, v157, v156
	s_waitcnt vmcnt(0)
	v_mfma_f32_16x16x32_f16 v[120:123], v[16:19], v[112:115], 0
	v_mfma_f32_16x16x32_f16 v[124:127], v[20:23], v[112:115], 0
	v_cndmask_b32_e32 v158, 4, v158, vcc
	v_mfma_f32_16x16x32_f16 v[128:131], v[24:27], v[112:115], 0
	v_mfma_f32_16x16x32_f16 v[132:135], v[28:31], v[112:115], 0
	v_min3_i32 v160, v136, v137, v157
	v_min3_i32 v160, v138, v139, v160
	v_min3_i32 v160, v140, v141, v160
	v_min3_i32 v160, v142, v143, v160
	v_min3_i32 v160, v144, v145, v160
	v_min3_i32 v160, v146, v147, v160
	v_min3_i32 v160, v148, v149, v160
	v_min3_i32 v156, v150, v151, v160
	v_cmp_ge_i32_e32 vcc, v156, v157
	v_mfma_f32_16x16x32_f16 v[136:139], v[32:35], v[112:115], 0
	v_mfma_f32_16x16x32_f16 v[140:143], v[36:39], v[112:115], 0
	v_cndmask_b32_e32 v158, 5, v158, vcc
	v_add_u32_e32 v162, s40, v158
	v_lshl_or_b32 v162, v162, 2, v166
	v_mov_b32_e32 v163, v156
	ds_min_u64 v167, v[162:163] offset:17280
	v_mfma_f32_16x16x32_f16 v[144:147], v[40:43], v[112:115], 0
	v_mfma_f32_16x16x32_f16 v[148:151], v[44:47], v[112:115], 0
	v_min3_i32 v160, v120, v121, s41
	v_min3_i32 v160, v122, v123, v160
	v_min3_i32 v160, v124, v125, v160
	v_min3_i32 v160, v126, v127, v160
	v_min3_i32 v160, v128, v129, v160
	v_min3_i32 v160, v130, v131, v160
	v_min3_i32 v160, v132, v133, v160
	v_min3_i32 v157, v134, v135, v160
	s_waitcnt lgkmcnt(0)
	s_barrier
	s_cmp_ge_u32 s50, 2
	s_cbranch_scc0 .Lp1a_z
	s_add_i32 s65, s50, 4
	s_lshl_b32 s60, s65, 7
	v_add_u32_e32 v2, s60, v169
	ds_read_b32 v216, v2 offset:16384
	s_lshl_b32 s60, s65, 10
	v_add_u32_e32 v248, s60, v170
.Lp1a_z:
	v_mfma_f32_16x16x32_f16 v[120:123], v[48:51], v[112:115], 0
	v_mfma_f32_16x16x32_f16 v[124:127], v[52:55], v[112:115], 0
	v_mov_b32_e32 v158, 0
	v_mfma_f32_16x16x32_f16 v[128:131], v[56:59], v[112:115], 0
	v_mfma_f32_16x16x32_f16 v[132:135], v[60:63], v[112:115], 0
	v_min3_i32 v160, v136, v137, v157
	v_min3_i32 v160, v138, v139, v160
	v_min3_i32 v160, v140, v141, v160
	v_min3_i32 v160, v142, v143, v160
	v_min3_i32 v160, v144, v145, v160
	v_min3_i32 v160, v146, v147, v160
	v_min3_i32 v160, v148, v149, v160
	v_min3_i32 v156, v150, v151, v160
	v_cmp_ge_i32_e32 vcc, v156, v157
	s_waitcnt lgkmcnt(0)
	s_cmp_ge_u32 s50, 2
	s_cbranch_scc0 .Lp1b_z
	v_lshrrev_b32_e32 v2, 2, v216
	v_mul_u32_u24_e32 v3, 43, v2
	v_lshrrev_b32_e32 v3, 8, v3
	v_mul_u32_u24_e32 v4, 6, v3
	v_sub_u32_e32 v4, v2, v4
	v_mul_u32_u24_e32 v3, 24, v3
	v_min_u32_e32 v3, 0xa5, v3
	v_lshl_add_u32 v3, v4, 2, v3
	v_lshrrev_b32_e32 v4, 2, v168
	v_add_u32_e32 v3, v3, v4
	v_and_b32_e32 v4, 3, v216
	v_lshlrev_b32_e32 v4, 2, v4
	v_and_b32_e32 v5, 3, v168
	v_or_b32_e32 v4, v4, v5
	v_lshl_or_b32 v252, v3, 4, v4
	v_add_u32_e32 v3, s9, v3
	v_lshlrev_b32_e32 v4, 4, v4
	v_lshl_or_b32 v244, v3, 10, v4
	global_load_dwordx4 v[216:219], v244, s[6:7]
	global_load_dwordx4 v[220:223], v244, s[6:7] offset:256
	global_load_dwordx4 v[224:227], v244, s[6:7] offset:512
	global_load_dwordx4 v[228:231], v244, s[6:7] offset:768
	global_load_dwordx4 v[232:235], v244, s[6:7] offset:2048
	global_load_dwordx4 v[236:239], v244, s[6:7] offset:2304
	global_load_dwordx4 v[240:243], v244, s[6:7] offset:2560
	global_load_dwordx4 v[244:247], v244, s[6:7] offset:2816
	global_load_dwordx4 v[248:251], v248, s[4:5]
.Lp1b_z:
	v_mfma_f32_16x16x32_f16 v[136:139], v[64:67], v[112:115], 0
	v_mfma_f32_16x16x32_f16 v[140:143], v[68:71], v[112:115], 0
	v_cndmask_b32_e32 v158, 1, v158, vcc
	v_mfma_f32_16x16x32_f16 v[144:147], v[72:75], v[112:115], 0
	v_mfma_f32_16x16x32_f16 v[148:151], v[76:79], v[112:115], 0
	v_min3_i32 v160, v120, v121, v156
	v_min3_i32 v160, v122, v123, v160
	v_min3_i32 v160, v124, v125, v160
	v_min3_i32 v160, v126, v127, v160
	v_min3_i32 v160, v128, v129, v160
	v_min3_i32 v160, v130, v131, v160
	v_min3_i32 v160, v132, v133, v160
	v_min3_i32 v157, v134, v135, v160
	v_cmp_ge_i32_e32 vcc, v157, v156
	v_mfma_f32_16x16x32_f16 v[120:123], v[80:83], v[112:115], 0
	v_mfma_f32_16x16x32_f16 v[124:127], v[84:87], v[112:115], 0
	v_cndmask_b32_e32 v158, 2, v158, vcc
	v_mfma_f32_16x16x32_f16 v[128:131], v[88:91], v[112:115], 0
	v_mfma_f32_16x16x32_f16 v[132:135], v[92:95], v[112:115], 0
	v_min3_i32 v160, v136, v137, v157
	v_min3_i32 v160, v138, v139, v160
	v_min3_i32 v160, v140, v141, v160
	v_min3_i32 v160, v142, v143, v160
	v_min3_i32 v160, v144, v145, v160
	v_min3_i32 v160, v146, v147, v160
	v_min3_i32 v160, v148, v149, v160
	v_min3_i32 v156, v150, v151, v160
	v_cmp_ge_i32_e32 vcc, v156, v157
	v_mfma_f32_16x16x32_f16 v[136:139], v[96:99], v[112:115], 0
	v_mfma_f32_16x16x32_f16 v[140:143], v[100:103], v[112:115], 0
	v_cndmask_b32_e32 v158, 3, v158, vcc
	v_mfma_f32_16x16x32_f16 v[144:147], v[104:107], v[112:115], 0
	v_mfma_f32_16x16x32_f16 v[148:151], v[108:111], v[112:115], 0
	v_min3_i32 v160, v120, v121, v156
	v_min3_i32 v160, v122, v123, v160
	v_min3_i32 v160, v124, v125, v160
	v_min3_i32 v160, v126, v127, v160
	v_min3_i32 v160, v128, v129, v160
	v_min3_i32 v160, v130, v131, v160
	v_min3_i32 v160, v132, v133, v160
	v_min3_i32 v157, v134, v135, v160
	v_cmp_ge_i32_e32 vcc, v157, v156
	s_nop 1
	v_cndmask_b32_e32 v158, 4, v158, vcc
	s_nop 7
	v_min3_i32 v160, v136, v137, v157
	v_min3_i32 v160, v138, v139, v160
	v_min3_i32 v160, v140, v141, v160
	v_min3_i32 v160, v142, v143, v160
	v_min3_i32 v160, v144, v145, v160
	v_min3_i32 v160, v146, v147, v160
	v_min3_i32 v160, v148, v149, v160
	v_min3_i32 v156, v150, v151, v160
	v_cmp_ge_i32_e32 vcc, v156, v157
	s_nop 1
	v_cndmask_b32_e32 v158, 5, v158, vcc
	v_add_u32_e32 v162, s40, v158
	v_lshl_or_b32 v162, v162, 2, v166
	v_mov_b32_e32 v163, v156
	ds_min_u64 v167, v[162:163] offset:17408
	s_waitcnt lgkmcnt(0)
	s_barrier
	s_add_i32 s65, s50, 4
	s_mov_b32 s66, 8
	s_cmp_eq_u32 s50, 0
	s_cbranch_scc0 .Lq2
	s_lshl_b32 s60, s66, 7
	v_add_u32_e32 v2, s60, v169
	ds_read_b32 v16, v2 offset:16384
	s_lshl_b32 s60, s66, 10
	v_add_u32_e32 v48, s60, v170
.Lq2:
	s_waitcnt lgkmcnt(0)
	s_cmp_eq_u32 s50, 0
	s_cbranch_scc0 .Lq4
	v_lshrrev_b32_e32 v2, 2, v16
	v_mul_u32_u24_e32 v3, 43, v2
	v_lshrrev_b32_e32 v3, 8, v3
	v_mul_u32_u24_e32 v4, 6, v3
	v_sub_u32_e32 v4, v2, v4
	v_mul_u32_u24_e32 v3, 24, v3
	v_min_u32_e32 v3, 0xa5, v3
	v_lshl_add_u32 v3, v4, 2, v3
	v_lshrrev_b32_e32 v4, 2, v168
	v_add_u32_e32 v3, v3, v4
	v_and_b32_e32 v4, 3, v16
	v_lshlrev_b32_e32 v4, 2, v4
	v_and_b32_e32 v5, 3, v168
	v_or_b32_e32 v4, v4, v5
	v_lshl_or_b32 v52, v3, 4, v4
	v_add_u32_e32 v3, s9, v3
	v_lshlrev_b32_e32 v4, 4, v4
	v_lshl_or_b32 v44, v3, 10, v4
	global_load_dwordx4 v[16:19], v44, s[6:7]
	global_load_dwordx4 v[20:23], v44, s[6:7] offset:256
	global_load_dwordx4 v[24:27], v44, s[6:7] offset:512
	global_load_dwordx4 v[28:31], v44, s[6:7] offset:768
	global_load_dwordx4 v[32:35], v44, s[6:7] offset:2048
	global_load_dwordx4 v[36:39], v44, s[6:7] offset:2304
	global_load_dwordx4 v[40:43], v44, s[6:7] offset:2560
	global_load_dwordx4 v[44:47], v44, s[6:7] offset:2816
	global_load_dwordx4 v[48:51], v48, s[4:5]
